# GEMM mainloops: the back-to-back s_setprio 0 / s_setprio 1 pairs between the two MFMA halves of a segment are removed (priority stays raised across the segment)
# baseline (speedup 1.0000x reference)
; #define PG8_STAGE(bufoff, gbase, voff) do { _Pragma("unroll") for (int _i = 0; _i < 2; ++_i) \
;         __builtin_amdgcn_global_load_lds((const unsigned*)((const char*)(gbase) + (voff)[_i]), (PG8_LAS unsigned*)(lds + (bufoff) + ldsw + _i * 8192), 16, 0, 0); } while (0)
; #define PG8_LDA(dst, b, h) do { _Pragma("unroll") for (int m = 0; m < 4; ++m) _Pragma("unroll") for (int k = 0; k < 2; ++k) dst[m][k] = *(const PG8_LAS bf16x8*)(lds + PG8_SA(b, h) + aoff + m * 2048 + k * 1024); } while (0)
; #define PG8_LDB(dst, b, h) do { _Pragma("unroll") for (int n = 0; n < 2; ++n) _Pragma("unroll") for (int k = 0; k < 2; ++k) dst[n][k] = *(const PG8_LAS bf16x8*)(lds + PG8_SB(b, h) + boff + n * 2048 + k * 1024); } while (0)
; #define PG8_MMA(ai, bj, At, Bt) do { __builtin_amdgcn_s_setprio(1); _Pragma("unroll") for (int m = 0; m < 4; ++m) _Pragma("unroll") for (int n = 0; n < 2; ++n) _Pragma("unroll") for (int k = 0; k < 2; ++k) \
;         acc[ai][bj][m][n] = __builtin_amdgcn_mfma_f32_16x16x32_bf16(Bt[n][k], At[m][k], acc[ai][bj][m][n], 0, 0, 0); __builtin_amdgcn_s_setprio(0); } while (0)
; #define PG8_WAIT_V(n) asm volatile("s_waitcnt vmcnt(" #n ")" ::: "memory")
; #define PG8_WAIT_L(n) asm volatile("s_waitcnt lgkmcnt(" #n ")" ::: "memory")
; #define PG8_BAR __builtin_amdgcn_s_barrier()
; #define PG8_SCHED __builtin_amdgcn_sched_barrier(0)
; template <class Epi, class Sched, bool ALIGN_EPI = false, bool SP2 = false>
; __device__ __forceinline__ void gemm_phase(PG8_LAS unsigned char* lds, const Gemm g, const Sched& S, const Epi& E, const int tid) {
;     ...
;             PG8_LDB(B0, 0, 0); PG8_LDB(B1, 0, 1); PG8_SCHED; PG8_LDA(At, 0, 0); PG8_STAGE(PG8_SA(1, 1), a1 + hstep, voffA);
;             PG8_WAIT_V(8); PG8_WAIT_L(0); PG8_BAR; PG8_MMA(0, 0, At, B0); PG8_MMA(0, 1, At, B1); PG8_BAR; PG8_SCHED;
;             PG8_LDA(At, 0, 1); PG8_STAGE(PG8_SB(0, 0), b2, voffB); PG8_STAGE(PG8_SB(0, 1), b2 + hstep, voffB); PG8_STAGE(PG8_SA(0, 0), a2, voffA);
.LBB0_170:
	s_add_u32 s26, s22, 0xfff80080
	s_addc_u32 s27, s23, -1
	s_add_i32 s55, 0, 0x10000
	s_cmp_eq_u32 s54, 28
	s_cselect_b32 s29, s15, s27
	s_cselect_b32 s28, s50, s26
	s_cselect_b32 s27, s13, s53
	s_cselect_b32 s26, s51, s52
	s_add_i32 s58, 0, 0x14000
	v_add_u32_e32 v158, s55, v147
	v_add_u32_e32 v174, s58, v147
	ds_read_b128 v[142:145], v158
	ds_read_b128 v[150:153], v158 offset:1024
	ds_read_b128 v[154:157], v158 offset:2048
	ds_read_b128 v[158:161], v158 offset:3072
	ds_read_b128 v[162:165], v174
	ds_read_b128 v[166:169], v174 offset:1024
	ds_read_b128 v[170:173], v174 offset:2048
	ds_read_b128 v[174:177], v174 offset:3072
	v_lshl_add_u64 v[196:197], s[22:23], 0, v[138:139]
	s_add_i32 m0, s43, 0xc000
	ds_read_b128 v[178:181], v149
	ds_read_b128 v[182:185], v149 offset:1024
	ds_read_b128 v[186:189], v149 offset:2048
	ds_read_b128 v[190:193], v149 offset:3072
	ds_read_b128 v[210:213], v149 offset:4096
	ds_read_b128 v[214:217], v149 offset:5120
	ds_read_b128 v[218:221], v149 offset:6144
	ds_read_b128 v[234:237], v149 offset:7168
	global_load_lds_dwordx4 v[196:197], off
	v_lshl_add_u64 v[196:197], s[22:23], 0, v[140:141]
	s_add_i32 m0, s43, 0xe000
	s_nop 0
	global_load_lds_dwordx4 v[196:197], off
	s_waitcnt vmcnt(8)
	s_waitcnt lgkmcnt(0)
	s_barrier
	s_setprio 1
	s_waitcnt lgkmcnt(0)
	v_mfma_f32_16x16x32_bf16 v[126:129], v[142:145], v[178:181], v[126:129]
	v_mfma_f32_16x16x32_bf16 v[122:125], v[154:157], v[178:181], v[122:125]
	v_mfma_f32_16x16x32_bf16 v[110:113], v[142:145], v[186:189], v[110:113]
	v_mfma_f32_16x16x32_bf16 v[106:109], v[154:157], v[186:189], v[106:109]
	v_mfma_f32_16x16x32_bf16 v[94:97], v[142:145], v[210:213], v[94:97]
	v_mfma_f32_16x16x32_bf16 v[90:93], v[154:157], v[210:213], v[90:93]
	v_mfma_f32_16x16x32_bf16 v[76:79], v[142:145], v[218:221], v[76:79]
	v_mfma_f32_16x16x32_bf16 v[72:75], v[154:157], v[218:221], v[72:75]
	v_mfma_f32_16x16x32_bf16 v[126:129], v[150:153], v[182:185], v[126:129]
	v_mfma_f32_16x16x32_bf16 v[122:125], v[158:161], v[182:185], v[122:125]
	v_mfma_f32_16x16x32_bf16 v[110:113], v[150:153], v[190:193], v[110:113]
	v_mfma_f32_16x16x32_bf16 v[106:109], v[158:161], v[190:193], v[106:109]
	v_mfma_f32_16x16x32_bf16 v[94:97], v[150:153], v[214:217], v[94:97]
	v_mfma_f32_16x16x32_bf16 v[90:93], v[158:161], v[214:217], v[90:93]
	v_mfma_f32_16x16x32_bf16 v[76:79], v[150:153], v[234:237], v[76:79]
	v_mfma_f32_16x16x32_bf16 v[72:75], v[158:161], v[234:237], v[72:75]
	v_mfma_f32_16x16x32_bf16 v[118:121], v[162:165], v[178:181], v[118:121]
	v_mfma_f32_16x16x32_bf16 v[114:117], v[170:173], v[178:181], v[114:117]
	v_mfma_f32_16x16x32_bf16 v[102:105], v[162:165], v[186:189], v[102:105]
	v_mfma_f32_16x16x32_bf16 v[98:101], v[170:173], v[186:189], v[98:101]
	v_mfma_f32_16x16x32_bf16 v[86:89], v[162:165], v[210:213], v[86:89]
	v_mfma_f32_16x16x32_bf16 v[82:85], v[170:173], v[210:213], v[82:85]
	v_mfma_f32_16x16x32_bf16 v[68:71], v[162:165], v[218:221], v[68:71]
	v_mfma_f32_16x16x32_bf16 v[64:67], v[170:173], v[218:221], v[64:67]
	v_mfma_f32_16x16x32_bf16 v[118:121], v[166:169], v[182:185], v[118:121]
	v_mfma_f32_16x16x32_bf16 v[114:117], v[174:177], v[182:185], v[114:117]
	v_mfma_f32_16x16x32_bf16 v[102:105], v[166:169], v[190:193], v[102:105]
	v_mfma_f32_16x16x32_bf16 v[98:101], v[174:177], v[190:193], v[98:101]
	v_mfma_f32_16x16x32_bf16 v[86:89], v[166:169], v[214:217], v[86:89]
	v_mfma_f32_16x16x32_bf16 v[82:85], v[174:177], v[214:217], v[82:85]
	v_mfma_f32_16x16x32_bf16 v[68:71], v[166:169], v[234:237], v[68:71]
	v_mfma_f32_16x16x32_bf16 v[64:67], v[174:177], v[234:237], v[64:67]
	s_setprio 0
	s_barrier
	s_add_i32 s55, s55, s42
	v_lshl_add_u64 v[196:197], s[26:27], 0, v[132:133]
	s_mov_b32 m0, s55
	ds_read_b128 v[178:181], v149 offset:16384
	ds_read_b128 v[182:185], v149 offset:17408
	ds_read_b128 v[186:189], v149 offset:18432
	ds_read_b128 v[190:193], v149 offset:19456
	ds_read_b128 v[210:213], v149 offset:20480
	ds_read_b128 v[214:217], v149 offset:21504
	ds_read_b128 v[218:221], v149 offset:22528
	ds_read_b128 v[234:237], v149 offset:23552
	global_load_lds_dwordx4 v[196:197], off
	s_add_i32 m0, s55, 0x2000
	s_add_u32 s56, s26, 0x80000
	v_lshl_add_u64 v[198:199], s[26:27], 0, v[136:137]
	s_addc_u32 s57, s27, 0
	s_add_i32 s55, s58, s42
	global_load_lds_dwordx4 v[198:199], off
	v_lshl_add_u64 v[206:207], s[56:57], 0, v[132:133]
	s_mov_b32 m0, s55
	v_lshl_add_u64 v[238:239], s[28:29], 0, v[134:135]
	global_load_lds_dwordx4 v[206:207], off
	v_lshl_add_u64 v[206:207], s[56:57], 0, v[136:137]
	s_add_i32 m0, s55, 0x2000
	s_nop 0
	global_load_lds_dwordx4 v[206:207], off
	v_lshl_add_u64 v[206:207], s[28:29], 0, v[130:131]
	s_mov_b32 m0, s43
	s_nop 0
	global_load_lds_dwordx4 v[206:207], off
	s_mov_b32 m0, s44
	s_nop 0
	global_load_lds_dwordx4 v[238:239], off
	s_waitcnt vmcnt(8)
	s_waitcnt lgkmcnt(0)
	s_barrier
; #define PG8_STAGE(bufoff, gbase, voff) do { _Pragma("unroll") for (int _i = 0; _i < 2; ++_i) \
;         __builtin_amdgcn_global_load_lds((const unsigned*)((const char*)(gbase) + (voff)[_i]), (PG8_LAS unsigned*)(lds + (bufoff) + ldsw + _i * 8192), 16, 0, 0); } while (0)
; #define PG8_LDA(dst, b, h) do { _Pragma("unroll") for (int m = 0; m < 4; ++m) _Pragma("unroll") for (int k = 0; k < 2; ++k) dst[m][k] = *(const PG8_LAS bf16x8*)(lds + PG8_SA(b, h) + aoff + m * 2048 + k * 1024); } while (0)
; #define PG8_LDB(dst, b, h) do { _Pragma("unroll") for (int n = 0; n < 2; ++n) _Pragma("unroll") for (int k = 0; k < 2; ++k) dst[n][k] = *(const PG8_LAS bf16x8*)(lds + PG8_SB(b, h) + boff + n * 2048 + k * 1024); } while (0)
; #define PG8_MMA(ai, bj, At, Bt) do { __builtin_amdgcn_s_setprio(1); _Pragma("unroll") for (int m = 0; m < 4; ++m) _Pragma("unroll") for (int n = 0; n < 2; ++n) _Pragma("unroll") for (int k = 0; k < 2; ++k) \
;         acc[ai][bj][m][n] = __builtin_amdgcn_mfma_f32_16x16x32_bf16(Bt[n][k], At[m][k], acc[ai][bj][m][n], 0, 0, 0); __builtin_amdgcn_s_setprio(0); } while (0)
; #define PG8_WAIT_V(n) asm volatile("s_waitcnt vmcnt(" #n ")" ::: "memory")
; #define PG8_WAIT_L(n) asm volatile("s_waitcnt lgkmcnt(" #n ")" ::: "memory")
; #define PG8_BAR __builtin_amdgcn_s_barrier()
; #define PG8_SCHED __builtin_amdgcn_sched_barrier(0)
; template <class Epi, class Sched, bool ALIGN_EPI = false, bool SP2 = false>
; __device__ __forceinline__ void gemm_phase(PG8_LAS unsigned char* lds, const Gemm g, const Sched& S, const Epi& E, const int tid) {
;     ...
;             PG8_WAIT_V(8); PG8_WAIT_L(0); PG8_BAR; PG8_MMA(1, 0, At, B0); PG8_MMA(1, 1, At, B1); PG8_BAR; PG8_SCHED;
;             PG8_LDB(B0, 1, 0); PG8_LDB(B1, 1, 1); PG8_SCHED; PG8_LDA(At, 1, 0); PG8_STAGE(PG8_SA(0, 1), a2 + hstep, voffA);
;             PG8_WAIT_V(8); PG8_WAIT_L(0); PG8_BAR; PG8_MMA(0, 0, At, B0); PG8_MMA(0, 1, At, B1); PG8_BAR; PG8_SCHED;
	s_setprio 1
	s_waitcnt lgkmcnt(0)
	v_mfma_f32_16x16x32_bf16 v[60:63], v[142:145], v[178:181], v[60:63]
	v_mfma_f32_16x16x32_bf16 v[56:59], v[154:157], v[178:181], v[56:59]
	v_mfma_f32_16x16x32_bf16 v[44:47], v[142:145], v[186:189], v[44:47]
	v_mfma_f32_16x16x32_bf16 v[40:43], v[154:157], v[186:189], v[40:43]
	v_mfma_f32_16x16x32_bf16 v[28:31], v[142:145], v[210:213], v[28:31]
	v_mfma_f32_16x16x32_bf16 v[24:27], v[154:157], v[210:213], v[24:27]
	v_mfma_f32_16x16x32_bf16 v[12:15], v[142:145], v[218:221], v[12:15]
	v_mfma_f32_16x16x32_bf16 v[8:11], v[154:157], v[218:221], v[8:11]
	v_mfma_f32_16x16x32_bf16 v[60:63], v[150:153], v[182:185], v[60:63]
	v_mfma_f32_16x16x32_bf16 v[56:59], v[158:161], v[182:185], v[56:59]
	v_mfma_f32_16x16x32_bf16 v[44:47], v[150:153], v[190:193], v[44:47]
	v_mfma_f32_16x16x32_bf16 v[40:43], v[158:161], v[190:193], v[40:43]
	v_mfma_f32_16x16x32_bf16 v[28:31], v[150:153], v[214:217], v[28:31]
	v_mfma_f32_16x16x32_bf16 v[24:27], v[158:161], v[214:217], v[24:27]
	v_mfma_f32_16x16x32_bf16 v[12:15], v[150:153], v[234:237], v[12:15]
	v_mfma_f32_16x16x32_bf16 v[8:11], v[158:161], v[234:237], v[8:11]
	v_mfma_f32_16x16x32_bf16 v[52:55], v[162:165], v[178:181], v[52:55]
	v_mfma_f32_16x16x32_bf16 v[48:51], v[170:173], v[178:181], v[48:51]
	v_mfma_f32_16x16x32_bf16 v[36:39], v[162:165], v[186:189], v[36:39]
	v_mfma_f32_16x16x32_bf16 v[32:35], v[170:173], v[186:189], v[32:35]
	v_mfma_f32_16x16x32_bf16 v[20:23], v[162:165], v[210:213], v[20:23]
	v_mfma_f32_16x16x32_bf16 v[16:19], v[170:173], v[210:213], v[16:19]
	v_mfma_f32_16x16x32_bf16 v[4:7], v[162:165], v[218:221], v[4:7]
	v_mfma_f32_16x16x32_bf16 v[0:3], v[170:173], v[218:221], v[0:3]
	v_mfma_f32_16x16x32_bf16 v[52:55], v[166:169], v[182:185], v[52:55]
	v_mfma_f32_16x16x32_bf16 v[48:51], v[174:177], v[182:185], v[48:51]
	v_mfma_f32_16x16x32_bf16 v[36:39], v[166:169], v[190:193], v[36:39]
	v_mfma_f32_16x16x32_bf16 v[32:35], v[174:177], v[190:193], v[32:35]
	v_mfma_f32_16x16x32_bf16 v[20:23], v[166:169], v[214:217], v[20:23]
	v_mfma_f32_16x16x32_bf16 v[16:19], v[174:177], v[214:217], v[16:19]
	v_mfma_f32_16x16x32_bf16 v[4:7], v[166:169], v[234:237], v[4:7]
	v_mfma_f32_16x16x32_bf16 v[0:3], v[174:177], v[234:237], v[0:3]
	s_setprio 0
	s_barrier
	s_add_i32 s55, 0, 0x18000
	s_add_i32 s56, 0, 0x1c000
	v_add_u32_e32 v158, s55, v147
	v_add_u32_e32 v174, s56, v147
	ds_read_b128 v[142:145], v158
	ds_read_b128 v[150:153], v158 offset:1024
	ds_read_b128 v[154:157], v158 offset:2048
	ds_read_b128 v[158:161], v158 offset:3072
	ds_read_b128 v[162:165], v174
	ds_read_b128 v[166:169], v174 offset:1024
	ds_read_b128 v[170:173], v174 offset:2048
	ds_read_b128 v[174:177], v174 offset:3072
	s_add_u32 s28, s28, 0x80000
	s_addc_u32 s29, s29, 0
	s_mov_b32 m0, s45
	v_lshl_add_u64 v[240:241], s[28:29], 0, v[130:131]
	ds_read_b128 v[178:181], v149 offset:32768
	ds_read_b128 v[182:185], v149 offset:33792
	ds_read_b128 v[186:189], v149 offset:34816
	ds_read_b128 v[190:193], v149 offset:35840
	ds_read_b128 v[210:213], v149 offset:36864
	ds_read_b128 v[214:217], v149 offset:37888
	ds_read_b128 v[218:221], v149 offset:38912
	ds_read_b128 v[234:237], v149 offset:39936
	global_load_lds_dwordx4 v[240:241], off
	v_lshl_add_u64 v[240:241], s[28:29], 0, v[134:135]
	s_mov_b32 m0, s46
	s_nop 0
	global_load_lds_dwordx4 v[240:241], off
	s_waitcnt vmcnt(8)
	s_waitcnt lgkmcnt(0)
	s_barrier
	s_setprio 1
	s_waitcnt lgkmcnt(0)
	v_mfma_f32_16x16x32_bf16 v[126:129], v[142:145], v[178:181], v[126:129]
	v_mfma_f32_16x16x32_bf16 v[122:125], v[154:157], v[178:181], v[122:125]
	v_mfma_f32_16x16x32_bf16 v[110:113], v[142:145], v[186:189], v[110:113]
	v_mfma_f32_16x16x32_bf16 v[106:109], v[154:157], v[186:189], v[106:109]
	v_mfma_f32_16x16x32_bf16 v[94:97], v[142:145], v[210:213], v[94:97]
	v_mfma_f32_16x16x32_bf16 v[90:93], v[154:157], v[210:213], v[90:93]
	v_mfma_f32_16x16x32_bf16 v[76:79], v[142:145], v[218:221], v[76:79]
	v_mfma_f32_16x16x32_bf16 v[72:75], v[154:157], v[218:221], v[72:75]
	v_mfma_f32_16x16x32_bf16 v[126:129], v[150:153], v[182:185], v[126:129]
	v_mfma_f32_16x16x32_bf16 v[122:125], v[158:161], v[182:185], v[122:125]
	v_mfma_f32_16x16x32_bf16 v[110:113], v[150:153], v[190:193], v[110:113]
	v_mfma_f32_16x16x32_bf16 v[106:109], v[158:161], v[190:193], v[106:109]
	v_mfma_f32_16x16x32_bf16 v[94:97], v[150:153], v[214:217], v[94:97]
	v_mfma_f32_16x16x32_bf16 v[90:93], v[158:161], v[214:217], v[90:93]
	v_mfma_f32_16x16x32_bf16 v[76:79], v[150:153], v[234:237], v[76:79]
	v_mfma_f32_16x16x32_bf16 v[72:75], v[158:161], v[234:237], v[72:75]
	v_mfma_f32_16x16x32_bf16 v[118:121], v[162:165], v[178:181], v[118:121]
	v_mfma_f32_16x16x32_bf16 v[114:117], v[170:173], v[178:181], v[114:117]
	v_mfma_f32_16x16x32_bf16 v[102:105], v[162:165], v[186:189], v[102:105]
	v_mfma_f32_16x16x32_bf16 v[98:101], v[170:173], v[186:189], v[98:101]
	v_mfma_f32_16x16x32_bf16 v[86:89], v[162:165], v[210:213], v[86:89]
	v_mfma_f32_16x16x32_bf16 v[82:85], v[170:173], v[210:213], v[82:85]
	v_mfma_f32_16x16x32_bf16 v[68:71], v[162:165], v[218:221], v[68:71]
	v_mfma_f32_16x16x32_bf16 v[64:67], v[170:173], v[218:221], v[64:67]
	v_mfma_f32_16x16x32_bf16 v[118:121], v[166:169], v[182:185], v[118:121]
	v_mfma_f32_16x16x32_bf16 v[114:117], v[174:177], v[182:185], v[114:117]
	v_mfma_f32_16x16x32_bf16 v[102:105], v[166:169], v[190:193], v[102:105]
	v_mfma_f32_16x16x32_bf16 v[98:101], v[174:177], v[190:193], v[98:101]
	v_mfma_f32_16x16x32_bf16 v[86:89], v[166:169], v[214:217], v[86:89]
	v_mfma_f32_16x16x32_bf16 v[82:85], v[174:177], v[214:217], v[82:85]
	v_mfma_f32_16x16x32_bf16 v[68:71], v[166:169], v[234:237], v[68:71]
	v_mfma_f32_16x16x32_bf16 v[64:67], v[174:177], v[234:237], v[64:67]
	s_setprio 0
	s_barrier
; #define PG8_STAGE(bufoff, gbase, voff) do { _Pragma("unroll") for (int _i = 0; _i < 2; ++_i) \
;         __builtin_amdgcn_global_load_lds((const unsigned*)((const char*)(gbase) + (voff)[_i]), (PG8_LAS unsigned*)(lds + (bufoff) + ldsw + _i * 8192), 16, 0, 0); } while (0)
; #define PG8_LDA(dst, b, h) do { _Pragma("unroll") for (int m = 0; m < 4; ++m) _Pragma("unroll") for (int k = 0; k < 2; ++k) dst[m][k] = *(const PG8_LAS bf16x8*)(lds + PG8_SA(b, h) + aoff + m * 2048 + k * 1024); } while (0)
; #define PG8_MMA(ai, bj, At, Bt) do { __builtin_amdgcn_s_setprio(1); _Pragma("unroll") for (int m = 0; m < 4; ++m) _Pragma("unroll") for (int n = 0; n < 2; ++n) _Pragma("unroll") for (int k = 0; k < 2; ++k) \
;         acc[ai][bj][m][n] = __builtin_amdgcn_mfma_f32_16x16x32_bf16(Bt[n][k], At[m][k], acc[ai][bj][m][n], 0, 0, 0); __builtin_amdgcn_s_setprio(0); } while (0)
; #define PG8_WAIT_V(n) asm volatile("s_waitcnt vmcnt(" #n ")" ::: "memory")
; #define PG8_WAIT_L(n) asm volatile("s_waitcnt lgkmcnt(" #n ")" ::: "memory")
; #define PG8_BAR __builtin_amdgcn_s_barrier()
; #define PG8_SCHED __builtin_amdgcn_sched_barrier(0)
; template <class Epi, class Sched, bool ALIGN_EPI = false, bool SP2 = false>
; __device__ __forceinline__ void gemm_phase(PG8_LAS unsigned char* lds, const Gemm g, const Sched& S, const Epi& E, const int tid) {
;     ...
;             PG8_LDA(At, 1, 1); PG8_STAGE(PG8_SB(1, 0), b3, voffB); PG8_STAGE(PG8_SB(1, 1), b3 + hstep, voffB); PG8_STAGE(PG8_SA(1, 0), a3, voffA);
;             PG8_WAIT_V(8); PG8_WAIT_L(0); PG8_BAR; PG8_MMA(1, 0, At, B0); PG8_MMA(1, 1, At, B1); PG8_BAR; PG8_SCHED;
;     ...
;         if constexpr (ALIGN_EPI) { if (wr == 0) PG8_BAR; }
	s_add_i32 s28, s55, s42
	v_lshl_add_u64 v[196:197], v[196:197], 0, s[20:21]
	s_mov_b32 m0, s28
	ds_read_b128 v[178:181], v149 offset:49152
	ds_read_b128 v[182:185], v149 offset:50176
	ds_read_b128 v[186:189], v149 offset:51200
	ds_read_b128 v[190:193], v149 offset:52224
	ds_read_b128 v[210:213], v149 offset:53248
	ds_read_b128 v[214:217], v149 offset:54272
	ds_read_b128 v[218:221], v149 offset:55296
	ds_read_b128 v[234:237], v149 offset:56320
	global_load_lds_dwordx4 v[196:197], off
	s_add_i32 m0, s28, 0x2000
	s_add_u32 s26, s26, 0x80080
	v_lshl_add_u64 v[196:197], v[198:199], 0, s[20:21]
	s_addc_u32 s27, s27, 0
	s_add_i32 s28, s56, s42
	global_load_lds_dwordx4 v[196:197], off
	v_lshl_add_u64 v[196:197], s[26:27], 0, v[132:133]
	s_mov_b32 m0, s28
	s_nop 0
	global_load_lds_dwordx4 v[196:197], off
	v_lshl_add_u64 v[196:197], s[26:27], 0, v[136:137]
	s_add_i32 m0, s28, 0x2000
	s_nop 0
	global_load_lds_dwordx4 v[196:197], off
	v_lshl_add_u64 v[196:197], v[206:207], 0, s[20:21]
	s_mov_b32 m0, s47
	s_nop 0
	global_load_lds_dwordx4 v[196:197], off
	v_lshl_add_u64 v[196:197], v[238:239], 0, s[20:21]
	s_mov_b32 m0, s48
	s_nop 0
	global_load_lds_dwordx4 v[196:197], off
	s_waitcnt vmcnt(8)
	s_waitcnt lgkmcnt(0)
	s_barrier
	s_setprio 1
	s_waitcnt lgkmcnt(0)
	v_mfma_f32_16x16x32_bf16 v[60:63], v[142:145], v[178:181], v[60:63]
	v_mfma_f32_16x16x32_bf16 v[56:59], v[154:157], v[178:181], v[56:59]
	v_mfma_f32_16x16x32_bf16 v[44:47], v[142:145], v[186:189], v[44:47]
	v_mfma_f32_16x16x32_bf16 v[40:43], v[154:157], v[186:189], v[40:43]
	v_mfma_f32_16x16x32_bf16 v[28:31], v[142:145], v[210:213], v[28:31]
	v_mfma_f32_16x16x32_bf16 v[24:27], v[154:157], v[210:213], v[24:27]
	v_mfma_f32_16x16x32_bf16 v[12:15], v[142:145], v[218:221], v[12:15]
	v_mfma_f32_16x16x32_bf16 v[8:11], v[154:157], v[218:221], v[8:11]
	v_mfma_f32_16x16x32_bf16 v[60:63], v[150:153], v[182:185], v[60:63]
	v_mfma_f32_16x16x32_bf16 v[56:59], v[158:161], v[182:185], v[56:59]
	v_mfma_f32_16x16x32_bf16 v[44:47], v[150:153], v[190:193], v[44:47]
	v_mfma_f32_16x16x32_bf16 v[40:43], v[158:161], v[190:193], v[40:43]
	v_mfma_f32_16x16x32_bf16 v[28:31], v[150:153], v[214:217], v[28:31]
	v_mfma_f32_16x16x32_bf16 v[24:27], v[158:161], v[214:217], v[24:27]
	v_mfma_f32_16x16x32_bf16 v[12:15], v[150:153], v[234:237], v[12:15]
	v_mfma_f32_16x16x32_bf16 v[8:11], v[158:161], v[234:237], v[8:11]
	v_mfma_f32_16x16x32_bf16 v[52:55], v[162:165], v[178:181], v[52:55]
	v_mfma_f32_16x16x32_bf16 v[48:51], v[170:173], v[178:181], v[48:51]
	v_mfma_f32_16x16x32_bf16 v[36:39], v[162:165], v[186:189], v[36:39]
	v_mfma_f32_16x16x32_bf16 v[32:35], v[170:173], v[186:189], v[32:35]
	v_mfma_f32_16x16x32_bf16 v[20:23], v[162:165], v[210:213], v[20:23]
	v_mfma_f32_16x16x32_bf16 v[16:19], v[170:173], v[210:213], v[16:19]
	v_mfma_f32_16x16x32_bf16 v[4:7], v[162:165], v[218:221], v[4:7]
	v_mfma_f32_16x16x32_bf16 v[0:3], v[170:173], v[218:221], v[0:3]
	v_mfma_f32_16x16x32_bf16 v[52:55], v[166:169], v[182:185], v[52:55]
	v_mfma_f32_16x16x32_bf16 v[48:51], v[174:177], v[182:185], v[48:51]
	v_mfma_f32_16x16x32_bf16 v[36:39], v[166:169], v[190:193], v[36:39]
	v_mfma_f32_16x16x32_bf16 v[32:35], v[174:177], v[190:193], v[32:35]
	v_mfma_f32_16x16x32_bf16 v[20:23], v[166:169], v[214:217], v[20:23]
	v_mfma_f32_16x16x32_bf16 v[16:19], v[174:177], v[214:217], v[16:19]
	v_mfma_f32_16x16x32_bf16 v[4:7], v[166:169], v[234:237], v[4:7]
	v_mfma_f32_16x16x32_bf16 v[0:3], v[174:177], v[234:237], v[0:3]
	s_setprio 0
	s_barrier
	s_add_i32 s54, s54, 2
	s_add_u32 s22, s22, 0x100
	s_addc_u32 s23, s23, 0
	s_add_u32 s52, s52, 0x100
	s_addc_u32 s53, s53, 0
	s_cmp_gt_u32 s54, 29
	s_cbranch_scc0 .LBB0_170
	s_and_b64 vcc, exec, s[10:11]
	s_cbranch_vccz .LBB0_173
	s_barrier

; #define PG8_STAGE(bufoff, gbase, voff) do { _Pragma("unroll") for (int _i = 0; _i < 2; ++_i) \
;         __builtin_amdgcn_global_load_lds((const unsigned*)((const char*)(gbase) + (voff)[_i]), (PG8_LAS unsigned*)(lds + (bufoff) + ldsw + _i * 8192), 16, 0, 0); } while (0)
; #define PG8_LDA(dst, b, h) do { _Pragma("unroll") for (int m = 0; m < 4; ++m) _Pragma("unroll") for (int k = 0; k < 2; ++k) dst[m][k] = *(const PG8_LAS bf16x8*)(lds + PG8_SA(b, h) + aoff + m * 2048 + k * 1024); } while (0)
; #define PG8_LDB(dst, b, h) do { _Pragma("unroll") for (int n = 0; n < 2; ++n) _Pragma("unroll") for (int k = 0; k < 2; ++k) dst[n][k] = *(const PG8_LAS bf16x8*)(lds + PG8_SB(b, h) + boff + n * 2048 + k * 1024); } while (0)
; #define PG8_MMA(ai, bj, At, Bt) do { __builtin_amdgcn_s_setprio(1); _Pragma("unroll") for (int m = 0; m < 4; ++m) _Pragma("unroll") for (int n = 0; n < 2; ++n) _Pragma("unroll") for (int k = 0; k < 2; ++k) \
;         acc[ai][bj][m][n] = __builtin_amdgcn_mfma_f32_16x16x32_bf16(Bt[n][k], At[m][k], acc[ai][bj][m][n], 0, 0, 0); __builtin_amdgcn_s_setprio(0); } while (0)
; #define PG8_WAIT_V(n) asm volatile("s_waitcnt vmcnt(" #n ")" ::: "memory")
; #define PG8_WAIT_L(n) asm volatile("s_waitcnt lgkmcnt(" #n ")" ::: "memory")
; #define PG8_BAR __builtin_amdgcn_s_barrier()
; #define PG8_SCHED __builtin_amdgcn_sched_barrier(0)
; template <class Epi, class Sched, bool ALIGN_EPI = false, bool SP2 = false>
; __device__ __forceinline__ void gemm_phase(PG8_LAS unsigned char* lds, const Gemm g, const Sched& S, const Epi& E, const int tid) {
;     ...
;             PG8_LDB(B0, 0, 0); PG8_LDB(B1, 0, 1); PG8_SCHED; PG8_LDA(At, 0, 0); PG8_STAGE(PG8_SA(1, 1), a1 + hstep, voffA);
;             PG8_WAIT_V(8); PG8_WAIT_L(0); PG8_BAR; PG8_MMA(0, 0, At, B0); PG8_MMA(0, 1, At, B1); PG8_BAR; PG8_SCHED;
;             PG8_LDA(At, 0, 1); PG8_STAGE(PG8_SB(0, 0), b2, voffB); PG8_STAGE(PG8_SB(0, 1), b2 + hstep, voffB); PG8_STAGE(PG8_SA(0, 0), a2, voffA);
.LBB0_646:
	s_add_u32 s26, s22, 0xfff80080
	s_addc_u32 s27, s23, -1
	s_add_i32 s56, 0, 0x10000
	s_cmp_eq_u32 s55, 28
	s_cselect_b32 s29, s15, s27
	s_cselect_b32 s28, s51, s26
	v_add_u32_e32 v146, s56, v148
	s_cselect_b32 s27, s13, s54
	s_cselect_b32 s26, s52, s53
	s_add_i32 s58, 0, 0x14000
	ds_read_b128 v[142:145], v146
	ds_read_b128 v[152:155], v146 offset:1024
	ds_read_b128 v[156:159], v146 offset:2048
	ds_read_b128 v[160:163], v146 offset:3072
	v_add_u32_e32 v146, s58, v148
	ds_read_b128 v[164:167], v146
	ds_read_b128 v[168:171], v146 offset:1024
	ds_read_b128 v[172:175], v146 offset:2048
	ds_read_b128 v[176:179], v146 offset:3072
	v_lshl_add_u64 v[146:147], s[22:23], 0, v[138:139]
	s_add_i32 m0, s42, 0xc000
	ds_read_b128 v[180:183], v150
	ds_read_b128 v[184:187], v150 offset:1024
	ds_read_b128 v[188:191], v150 offset:2048
	ds_read_b128 v[210:213], v150 offset:3072
	ds_read_b128 v[214:217], v150 offset:4096
	ds_read_b128 v[218:221], v150 offset:5120
	ds_read_b128 v[234:237], v150 offset:6144
	ds_read_b128 v[238:241], v150 offset:7168
	global_load_lds_dwordx4 v[146:147], off
	v_lshl_add_u64 v[146:147], s[22:23], 0, v[140:141]
	s_add_i32 m0, s42, 0xe000
	s_nop 0
	global_load_lds_dwordx4 v[146:147], off
	s_waitcnt vmcnt(8)
	s_waitcnt lgkmcnt(0)
	s_barrier
	s_setprio 1
	s_waitcnt lgkmcnt(0)
	v_mfma_f32_16x16x32_bf16 v[126:129], v[142:145], v[180:183], v[126:129]
	v_mfma_f32_16x16x32_bf16 v[122:125], v[156:159], v[180:183], v[122:125]
	v_mfma_f32_16x16x32_bf16 v[110:113], v[142:145], v[188:191], v[110:113]
	v_mfma_f32_16x16x32_bf16 v[106:109], v[156:159], v[188:191], v[106:109]
	v_mfma_f32_16x16x32_bf16 v[94:97], v[142:145], v[214:217], v[94:97]
	v_mfma_f32_16x16x32_bf16 v[90:93], v[156:159], v[214:217], v[90:93]
	v_mfma_f32_16x16x32_bf16 v[76:79], v[142:145], v[234:237], v[76:79]
	v_mfma_f32_16x16x32_bf16 v[72:75], v[156:159], v[234:237], v[72:75]
	v_mfma_f32_16x16x32_bf16 v[126:129], v[152:155], v[184:187], v[126:129]
	v_mfma_f32_16x16x32_bf16 v[122:125], v[160:163], v[184:187], v[122:125]
	v_mfma_f32_16x16x32_bf16 v[110:113], v[152:155], v[210:213], v[110:113]
	v_mfma_f32_16x16x32_bf16 v[106:109], v[160:163], v[210:213], v[106:109]
	v_mfma_f32_16x16x32_bf16 v[94:97], v[152:155], v[218:221], v[94:97]
	v_mfma_f32_16x16x32_bf16 v[90:93], v[160:163], v[218:221], v[90:93]
	v_mfma_f32_16x16x32_bf16 v[76:79], v[152:155], v[238:241], v[76:79]
	v_mfma_f32_16x16x32_bf16 v[72:75], v[160:163], v[238:241], v[72:75]
	v_mfma_f32_16x16x32_bf16 v[118:121], v[164:167], v[180:183], v[118:121]
	v_mfma_f32_16x16x32_bf16 v[114:117], v[172:175], v[180:183], v[114:117]
	v_mfma_f32_16x16x32_bf16 v[102:105], v[164:167], v[188:191], v[102:105]
	v_mfma_f32_16x16x32_bf16 v[98:101], v[172:175], v[188:191], v[98:101]
	v_mfma_f32_16x16x32_bf16 v[86:89], v[164:167], v[214:217], v[86:89]
	v_mfma_f32_16x16x32_bf16 v[82:85], v[172:175], v[214:217], v[82:85]
	v_mfma_f32_16x16x32_bf16 v[68:71], v[164:167], v[234:237], v[68:71]
	v_mfma_f32_16x16x32_bf16 v[64:67], v[172:175], v[234:237], v[64:67]
	v_mfma_f32_16x16x32_bf16 v[118:121], v[168:171], v[184:187], v[118:121]
	v_mfma_f32_16x16x32_bf16 v[114:117], v[176:179], v[184:187], v[114:117]
	v_mfma_f32_16x16x32_bf16 v[102:105], v[168:171], v[210:213], v[102:105]
	v_mfma_f32_16x16x32_bf16 v[98:101], v[176:179], v[210:213], v[98:101]
	v_mfma_f32_16x16x32_bf16 v[86:89], v[168:171], v[218:221], v[86:89]
	v_mfma_f32_16x16x32_bf16 v[82:85], v[176:179], v[218:221], v[82:85]
	v_mfma_f32_16x16x32_bf16 v[68:71], v[168:171], v[238:241], v[68:71]
	v_mfma_f32_16x16x32_bf16 v[64:67], v[176:179], v[238:241], v[64:67]
	s_setprio 0
	s_barrier
	s_add_i32 s56, s56, s36
	v_lshl_add_u64 v[146:147], s[26:27], 0, v[132:133]
	s_mov_b32 m0, s56
	ds_read_b128 v[180:183], v150 offset:16384
	ds_read_b128 v[184:187], v150 offset:17408
	ds_read_b128 v[188:191], v150 offset:18432
	ds_read_b128 v[210:213], v150 offset:19456
	ds_read_b128 v[214:217], v150 offset:20480
	ds_read_b128 v[218:221], v150 offset:21504
	ds_read_b128 v[234:237], v150 offset:22528
	ds_read_b128 v[238:241], v150 offset:23552
	global_load_lds_dwordx4 v[146:147], off
	s_add_i32 m0, s56, 0x2000
	s_add_u32 s56, s26, 0x80000
	v_lshl_add_u64 v[192:193], s[26:27], 0, v[136:137]
	s_addc_u32 s57, s27, 0
	s_add_i32 s58, s58, s36
	global_load_lds_dwordx4 v[192:193], off
	v_lshl_add_u64 v[196:197], s[56:57], 0, v[132:133]
	s_mov_b32 m0, s58
	v_lshl_add_u64 v[198:199], s[28:29], 0, v[134:135]
	global_load_lds_dwordx4 v[196:197], off
	v_lshl_add_u64 v[196:197], s[56:57], 0, v[136:137]
	s_add_i32 m0, s58, 0x2000
	s_nop 0
	global_load_lds_dwordx4 v[196:197], off
	v_lshl_add_u64 v[196:197], s[28:29], 0, v[130:131]
	s_mov_b32 m0, s42
	s_nop 0
	global_load_lds_dwordx4 v[196:197], off
	s_mov_b32 m0, s43
	s_nop 0
	global_load_lds_dwordx4 v[198:199], off
	s_waitcnt vmcnt(8)
	s_waitcnt lgkmcnt(0)
	s_barrier
; #define PG8_STAGE(bufoff, gbase, voff) do { _Pragma("unroll") for (int _i = 0; _i < 2; ++_i) \
;         __builtin_amdgcn_global_load_lds((const unsigned*)((const char*)(gbase) + (voff)[_i]), (PG8_LAS unsigned*)(lds + (bufoff) + ldsw + _i * 8192), 16, 0, 0); } while (0)
; #define PG8_LDA(dst, b, h) do { _Pragma("unroll") for (int m = 0; m < 4; ++m) _Pragma("unroll") for (int k = 0; k < 2; ++k) dst[m][k] = *(const PG8_LAS bf16x8*)(lds + PG8_SA(b, h) + aoff + m * 2048 + k * 1024); } while (0)
; #define PG8_LDB(dst, b, h) do { _Pragma("unroll") for (int n = 0; n < 2; ++n) _Pragma("unroll") for (int k = 0; k < 2; ++k) dst[n][k] = *(const PG8_LAS bf16x8*)(lds + PG8_SB(b, h) + boff + n * 2048 + k * 1024); } while (0)
; #define PG8_MMA(ai, bj, At, Bt) do { __builtin_amdgcn_s_setprio(1); _Pragma("unroll") for (int m = 0; m < 4; ++m) _Pragma("unroll") for (int n = 0; n < 2; ++n) _Pragma("unroll") for (int k = 0; k < 2; ++k) \
;         acc[ai][bj][m][n] = __builtin_amdgcn_mfma_f32_16x16x32_bf16(Bt[n][k], At[m][k], acc[ai][bj][m][n], 0, 0, 0); __builtin_amdgcn_s_setprio(0); } while (0)
; #define PG8_WAIT_V(n) asm volatile("s_waitcnt vmcnt(" #n ")" ::: "memory")
; #define PG8_WAIT_L(n) asm volatile("s_waitcnt lgkmcnt(" #n ")" ::: "memory")
; #define PG8_BAR __builtin_amdgcn_s_barrier()
; #define PG8_SCHED __builtin_amdgcn_sched_barrier(0)
; template <class Epi, class Sched, bool ALIGN_EPI = false, bool SP2 = false>
; __device__ __forceinline__ void gemm_phase(PG8_LAS unsigned char* lds, const Gemm g, const Sched& S, const Epi& E, const int tid) {
;     ...
;             PG8_WAIT_V(8); PG8_WAIT_L(0); PG8_BAR; PG8_MMA(1, 0, At, B0); PG8_MMA(1, 1, At, B1); PG8_BAR; PG8_SCHED;
;             PG8_LDB(B0, 1, 0); PG8_LDB(B1, 1, 1); PG8_SCHED; PG8_LDA(At, 1, 0); PG8_STAGE(PG8_SA(0, 1), a2 + hstep, voffA);
;             PG8_WAIT_V(8); PG8_WAIT_L(0); PG8_BAR; PG8_MMA(0, 0, At, B0); PG8_MMA(0, 1, At, B1); PG8_BAR; PG8_SCHED;
	s_setprio 1
	s_waitcnt lgkmcnt(0)
	v_mfma_f32_16x16x32_bf16 v[60:63], v[142:145], v[180:183], v[60:63]
	v_mfma_f32_16x16x32_bf16 v[56:59], v[156:159], v[180:183], v[56:59]
	v_mfma_f32_16x16x32_bf16 v[44:47], v[142:145], v[188:191], v[44:47]
	v_mfma_f32_16x16x32_bf16 v[40:43], v[156:159], v[188:191], v[40:43]
	v_mfma_f32_16x16x32_bf16 v[28:31], v[142:145], v[214:217], v[28:31]
	v_mfma_f32_16x16x32_bf16 v[24:27], v[156:159], v[214:217], v[24:27]
	v_mfma_f32_16x16x32_bf16 v[12:15], v[142:145], v[234:237], v[12:15]
	v_mfma_f32_16x16x32_bf16 v[8:11], v[156:159], v[234:237], v[8:11]
	v_mfma_f32_16x16x32_bf16 v[60:63], v[152:155], v[184:187], v[60:63]
	v_mfma_f32_16x16x32_bf16 v[56:59], v[160:163], v[184:187], v[56:59]
	v_mfma_f32_16x16x32_bf16 v[44:47], v[152:155], v[210:213], v[44:47]
	v_mfma_f32_16x16x32_bf16 v[40:43], v[160:163], v[210:213], v[40:43]
	v_mfma_f32_16x16x32_bf16 v[28:31], v[152:155], v[218:221], v[28:31]
	v_mfma_f32_16x16x32_bf16 v[24:27], v[160:163], v[218:221], v[24:27]
	v_mfma_f32_16x16x32_bf16 v[12:15], v[152:155], v[238:241], v[12:15]
	v_mfma_f32_16x16x32_bf16 v[8:11], v[160:163], v[238:241], v[8:11]
	v_mfma_f32_16x16x32_bf16 v[52:55], v[164:167], v[180:183], v[52:55]
	v_mfma_f32_16x16x32_bf16 v[48:51], v[172:175], v[180:183], v[48:51]
	v_mfma_f32_16x16x32_bf16 v[36:39], v[164:167], v[188:191], v[36:39]
	v_mfma_f32_16x16x32_bf16 v[32:35], v[172:175], v[188:191], v[32:35]
	v_mfma_f32_16x16x32_bf16 v[20:23], v[164:167], v[214:217], v[20:23]
	v_mfma_f32_16x16x32_bf16 v[16:19], v[172:175], v[214:217], v[16:19]
	v_mfma_f32_16x16x32_bf16 v[4:7], v[164:167], v[234:237], v[4:7]
	v_mfma_f32_16x16x32_bf16 v[0:3], v[172:175], v[234:237], v[0:3]
	v_mfma_f32_16x16x32_bf16 v[52:55], v[168:171], v[184:187], v[52:55]
	v_mfma_f32_16x16x32_bf16 v[48:51], v[176:179], v[184:187], v[48:51]
	v_mfma_f32_16x16x32_bf16 v[36:39], v[168:171], v[210:213], v[36:39]
	v_mfma_f32_16x16x32_bf16 v[32:35], v[176:179], v[210:213], v[32:35]
	v_mfma_f32_16x16x32_bf16 v[20:23], v[168:171], v[218:221], v[20:23]
	v_mfma_f32_16x16x32_bf16 v[16:19], v[176:179], v[218:221], v[16:19]
	v_mfma_f32_16x16x32_bf16 v[4:7], v[168:171], v[238:241], v[4:7]
	v_mfma_f32_16x16x32_bf16 v[0:3], v[176:179], v[238:241], v[0:3]
	s_setprio 0
	s_barrier
	s_add_i32 s56, 0, 0x18000
	v_add_u32_e32 v151, s56, v148
	s_add_i32 s57, 0, 0x1c000
	ds_read_b128 v[142:145], v151
	ds_read_b128 v[152:155], v151 offset:1024
	ds_read_b128 v[156:159], v151 offset:2048
	ds_read_b128 v[160:163], v151 offset:3072
	v_add_u32_e32 v151, s57, v148
	ds_read_b128 v[164:167], v151
	ds_read_b128 v[168:171], v151 offset:1024
	ds_read_b128 v[172:175], v151 offset:2048
	ds_read_b128 v[176:179], v151 offset:3072
	s_add_u32 s28, s28, 0x80000
	s_addc_u32 s29, s29, 0
	s_mov_b32 m0, s44
	v_lshl_add_u64 v[206:207], s[28:29], 0, v[130:131]
	ds_read_b128 v[180:183], v150 offset:32768
	ds_read_b128 v[184:187], v150 offset:33792
	ds_read_b128 v[188:191], v150 offset:34816
	ds_read_b128 v[210:213], v150 offset:35840
	ds_read_b128 v[214:217], v150 offset:36864
	ds_read_b128 v[218:221], v150 offset:37888
	ds_read_b128 v[234:237], v150 offset:38912
	ds_read_b128 v[238:241], v150 offset:39936
	global_load_lds_dwordx4 v[206:207], off
	v_lshl_add_u64 v[206:207], s[28:29], 0, v[134:135]
	s_mov_b32 m0, s45
	s_nop 0
	global_load_lds_dwordx4 v[206:207], off
	s_waitcnt vmcnt(8)
	s_waitcnt lgkmcnt(0)
	s_barrier
	s_setprio 1
	s_waitcnt lgkmcnt(0)
	v_mfma_f32_16x16x32_bf16 v[126:129], v[142:145], v[180:183], v[126:129]
	v_mfma_f32_16x16x32_bf16 v[122:125], v[156:159], v[180:183], v[122:125]
	v_mfma_f32_16x16x32_bf16 v[110:113], v[142:145], v[188:191], v[110:113]
	v_mfma_f32_16x16x32_bf16 v[106:109], v[156:159], v[188:191], v[106:109]
	v_mfma_f32_16x16x32_bf16 v[94:97], v[142:145], v[214:217], v[94:97]
	v_mfma_f32_16x16x32_bf16 v[90:93], v[156:159], v[214:217], v[90:93]
	v_mfma_f32_16x16x32_bf16 v[76:79], v[142:145], v[234:237], v[76:79]
	v_mfma_f32_16x16x32_bf16 v[72:75], v[156:159], v[234:237], v[72:75]
	v_mfma_f32_16x16x32_bf16 v[126:129], v[152:155], v[184:187], v[126:129]
	v_mfma_f32_16x16x32_bf16 v[122:125], v[160:163], v[184:187], v[122:125]
	v_mfma_f32_16x16x32_bf16 v[110:113], v[152:155], v[210:213], v[110:113]
	v_mfma_f32_16x16x32_bf16 v[106:109], v[160:163], v[210:213], v[106:109]
	v_mfma_f32_16x16x32_bf16 v[94:97], v[152:155], v[218:221], v[94:97]
	v_mfma_f32_16x16x32_bf16 v[90:93], v[160:163], v[218:221], v[90:93]
	v_mfma_f32_16x16x32_bf16 v[76:79], v[152:155], v[238:241], v[76:79]
	v_mfma_f32_16x16x32_bf16 v[72:75], v[160:163], v[238:241], v[72:75]
	v_mfma_f32_16x16x32_bf16 v[118:121], v[164:167], v[180:183], v[118:121]
	v_mfma_f32_16x16x32_bf16 v[114:117], v[172:175], v[180:183], v[114:117]
	v_mfma_f32_16x16x32_bf16 v[102:105], v[164:167], v[188:191], v[102:105]
	v_mfma_f32_16x16x32_bf16 v[98:101], v[172:175], v[188:191], v[98:101]
	v_mfma_f32_16x16x32_bf16 v[86:89], v[164:167], v[214:217], v[86:89]
	v_mfma_f32_16x16x32_bf16 v[82:85], v[172:175], v[214:217], v[82:85]
	v_mfma_f32_16x16x32_bf16 v[68:71], v[164:167], v[234:237], v[68:71]
	v_mfma_f32_16x16x32_bf16 v[64:67], v[172:175], v[234:237], v[64:67]
	v_mfma_f32_16x16x32_bf16 v[118:121], v[168:171], v[184:187], v[118:121]
	v_mfma_f32_16x16x32_bf16 v[114:117], v[176:179], v[184:187], v[114:117]
	v_mfma_f32_16x16x32_bf16 v[102:105], v[168:171], v[210:213], v[102:105]
	v_mfma_f32_16x16x32_bf16 v[98:101], v[176:179], v[210:213], v[98:101]
	v_mfma_f32_16x16x32_bf16 v[86:89], v[168:171], v[218:221], v[86:89]
	v_mfma_f32_16x16x32_bf16 v[82:85], v[176:179], v[218:221], v[82:85]
	v_mfma_f32_16x16x32_bf16 v[68:71], v[168:171], v[238:241], v[68:71]
	v_mfma_f32_16x16x32_bf16 v[64:67], v[176:179], v[238:241], v[64:67]
	s_setprio 0
	s_barrier
; #define PG8_STAGE(bufoff, gbase, voff) do { _Pragma("unroll") for (int _i = 0; _i < 2; ++_i) \
;         __builtin_amdgcn_global_load_lds((const unsigned*)((const char*)(gbase) + (voff)[_i]), (PG8_LAS unsigned*)(lds + (bufoff) + ldsw + _i * 8192), 16, 0, 0); } while (0)
; #define PG8_LDA(dst, b, h) do { _Pragma("unroll") for (int m = 0; m < 4; ++m) _Pragma("unroll") for (int k = 0; k < 2; ++k) dst[m][k] = *(const PG8_LAS bf16x8*)(lds + PG8_SA(b, h) + aoff + m * 2048 + k * 1024); } while (0)
; #define PG8_MMA(ai, bj, At, Bt) do { __builtin_amdgcn_s_setprio(1); _Pragma("unroll") for (int m = 0; m < 4; ++m) _Pragma("unroll") for (int n = 0; n < 2; ++n) _Pragma("unroll") for (int k = 0; k < 2; ++k) \
;         acc[ai][bj][m][n] = __builtin_amdgcn_mfma_f32_16x16x32_bf16(Bt[n][k], At[m][k], acc[ai][bj][m][n], 0, 0, 0); __builtin_amdgcn_s_setprio(0); } while (0)
; #define PG8_WAIT_V(n) asm volatile("s_waitcnt vmcnt(" #n ")" ::: "memory")
; #define PG8_WAIT_L(n) asm volatile("s_waitcnt lgkmcnt(" #n ")" ::: "memory")
; #define PG8_BAR __builtin_amdgcn_s_barrier()
; #define PG8_SCHED __builtin_amdgcn_sched_barrier(0)
; template <class Epi, class Sched, bool ALIGN_EPI = false, bool SP2 = false>
; __device__ __forceinline__ void gemm_phase(PG8_LAS unsigned char* lds, const Gemm g, const Sched& S, const Epi& E, const int tid) {
;     ...
;             PG8_LDA(At, 1, 1); PG8_STAGE(PG8_SB(1, 0), b3, voffB); PG8_STAGE(PG8_SB(1, 1), b3 + hstep, voffB); PG8_STAGE(PG8_SA(1, 0), a3, voffA);
;             PG8_WAIT_V(8); PG8_WAIT_L(0); PG8_BAR; PG8_MMA(1, 0, At, B0); PG8_MMA(1, 1, At, B1); PG8_BAR; PG8_SCHED;
;     ...
;         if constexpr (ALIGN_EPI) { if (wr == 0) PG8_BAR; }
	s_add_i32 s28, s56, s36
	v_lshl_add_u64 v[146:147], v[146:147], 0, s[20:21]
	s_mov_b32 m0, s28
	ds_read_b128 v[180:183], v150 offset:49152
	ds_read_b128 v[184:187], v150 offset:50176
	ds_read_b128 v[188:191], v150 offset:51200
	ds_read_b128 v[210:213], v150 offset:52224
	ds_read_b128 v[214:217], v150 offset:53248
	ds_read_b128 v[218:221], v150 offset:54272
	ds_read_b128 v[234:237], v150 offset:55296
	ds_read_b128 v[238:241], v150 offset:56320
	global_load_lds_dwordx4 v[146:147], off
	s_add_i32 m0, s28, 0x2000
	s_add_u32 s26, s26, 0x80080
	v_lshl_add_u64 v[146:147], v[192:193], 0, s[20:21]
	s_addc_u32 s27, s27, 0
	s_add_i32 s28, s57, s36
	global_load_lds_dwordx4 v[146:147], off
	v_lshl_add_u64 v[146:147], s[26:27], 0, v[132:133]
	s_mov_b32 m0, s28
	s_nop 0
	global_load_lds_dwordx4 v[146:147], off
	v_lshl_add_u64 v[146:147], s[26:27], 0, v[136:137]
	s_add_i32 m0, s28, 0x2000
	s_nop 0
	global_load_lds_dwordx4 v[146:147], off
	v_lshl_add_u64 v[146:147], v[196:197], 0, s[20:21]
	s_mov_b32 m0, s46
	s_nop 0
	global_load_lds_dwordx4 v[146:147], off
	v_lshl_add_u64 v[146:147], v[198:199], 0, s[20:21]
	s_mov_b32 m0, s47
	s_nop 0
	global_load_lds_dwordx4 v[146:147], off
	s_waitcnt vmcnt(8)
	s_waitcnt lgkmcnt(0)
	s_barrier
	s_setprio 1
	s_waitcnt lgkmcnt(0)
	v_mfma_f32_16x16x32_bf16 v[60:63], v[142:145], v[180:183], v[60:63]
	v_mfma_f32_16x16x32_bf16 v[56:59], v[156:159], v[180:183], v[56:59]
	v_mfma_f32_16x16x32_bf16 v[44:47], v[142:145], v[188:191], v[44:47]
	v_mfma_f32_16x16x32_bf16 v[40:43], v[156:159], v[188:191], v[40:43]
	v_mfma_f32_16x16x32_bf16 v[28:31], v[142:145], v[214:217], v[28:31]
	v_mfma_f32_16x16x32_bf16 v[24:27], v[156:159], v[214:217], v[24:27]
	v_mfma_f32_16x16x32_bf16 v[12:15], v[142:145], v[234:237], v[12:15]
	v_mfma_f32_16x16x32_bf16 v[8:11], v[156:159], v[234:237], v[8:11]
	v_mfma_f32_16x16x32_bf16 v[60:63], v[152:155], v[184:187], v[60:63]
	v_mfma_f32_16x16x32_bf16 v[56:59], v[160:163], v[184:187], v[56:59]
	v_mfma_f32_16x16x32_bf16 v[44:47], v[152:155], v[210:213], v[44:47]
	v_mfma_f32_16x16x32_bf16 v[40:43], v[160:163], v[210:213], v[40:43]
	v_mfma_f32_16x16x32_bf16 v[28:31], v[152:155], v[218:221], v[28:31]
	v_mfma_f32_16x16x32_bf16 v[24:27], v[160:163], v[218:221], v[24:27]
	v_mfma_f32_16x16x32_bf16 v[12:15], v[152:155], v[238:241], v[12:15]
	v_mfma_f32_16x16x32_bf16 v[8:11], v[160:163], v[238:241], v[8:11]
	v_mfma_f32_16x16x32_bf16 v[52:55], v[164:167], v[180:183], v[52:55]
	v_mfma_f32_16x16x32_bf16 v[48:51], v[172:175], v[180:183], v[48:51]
	v_mfma_f32_16x16x32_bf16 v[36:39], v[164:167], v[188:191], v[36:39]
	v_mfma_f32_16x16x32_bf16 v[32:35], v[172:175], v[188:191], v[32:35]
	v_mfma_f32_16x16x32_bf16 v[20:23], v[164:167], v[214:217], v[20:23]
	v_mfma_f32_16x16x32_bf16 v[16:19], v[172:175], v[214:217], v[16:19]
	v_mfma_f32_16x16x32_bf16 v[4:7], v[164:167], v[234:237], v[4:7]
	v_mfma_f32_16x16x32_bf16 v[0:3], v[172:175], v[234:237], v[0:3]
	v_mfma_f32_16x16x32_bf16 v[52:55], v[168:171], v[184:187], v[52:55]
	v_mfma_f32_16x16x32_bf16 v[48:51], v[176:179], v[184:187], v[48:51]
	v_mfma_f32_16x16x32_bf16 v[36:39], v[168:171], v[210:213], v[36:39]
	v_mfma_f32_16x16x32_bf16 v[32:35], v[176:179], v[210:213], v[32:35]
	v_mfma_f32_16x16x32_bf16 v[20:23], v[168:171], v[218:221], v[20:23]
	v_mfma_f32_16x16x32_bf16 v[16:19], v[176:179], v[218:221], v[16:19]
	v_mfma_f32_16x16x32_bf16 v[4:7], v[168:171], v[238:241], v[4:7]
	v_mfma_f32_16x16x32_bf16 v[0:3], v[176:179], v[238:241], v[0:3]
	s_setprio 0
	s_barrier
	s_add_i32 s55, s55, 2
	s_add_u32 s22, s22, 0x100
	s_addc_u32 s23, s23, 0
	s_add_u32 s53, s53, 0x100
	s_addc_u32 s54, s54, 0
	s_cmp_gt_u32 s55, 29
	s_cbranch_scc0 .LBB0_646
	v_readlane_b32 s28, v254, 35
	s_and_b64 vcc, exec, s[10:11]
	s_mov_b32 s51, 0x5040100
	v_readlane_b32 s29, v254, 36
	s_mov_b64 s[54:55], 0x40000
	s_cbranch_vccz .LBB0_649
	s_barrier

; #define PG8_STAGE(bufoff, gbase, voff) do { _Pragma("unroll") for (int _i = 0; _i < 2; ++_i) \
;         __builtin_amdgcn_global_load_lds((const unsigned*)((const char*)(gbase) + (voff)[_i]), (PG8_LAS unsigned*)(lds + (bufoff) + ldsw + _i * 8192), 16, 0, 0); } while (0)
; #define PG8_LDA(dst, b, h) do { _Pragma("unroll") for (int m = 0; m < 4; ++m) _Pragma("unroll") for (int k = 0; k < 2; ++k) dst[m][k] = *(const PG8_LAS bf16x8*)(lds + PG8_SA(b, h) + aoff + m * 2048 + k * 1024); } while (0)
; #define PG8_LDB(dst, b, h) do { _Pragma("unroll") for (int n = 0; n < 2; ++n) _Pragma("unroll") for (int k = 0; k < 2; ++k) dst[n][k] = *(const PG8_LAS bf16x8*)(lds + PG8_SB(b, h) + boff + n * 2048 + k * 1024); } while (0)
; #define PG8_MMA(ai, bj, At, Bt) do { __builtin_amdgcn_s_setprio(1); _Pragma("unroll") for (int m = 0; m < 4; ++m) _Pragma("unroll") for (int n = 0; n < 2; ++n) _Pragma("unroll") for (int k = 0; k < 2; ++k) \
;         acc[ai][bj][m][n] = __builtin_amdgcn_mfma_f32_16x16x32_bf16(Bt[n][k], At[m][k], acc[ai][bj][m][n], 0, 0, 0); __builtin_amdgcn_s_setprio(0); } while (0)
; #define PG8_WAIT_V(n) asm volatile("s_waitcnt vmcnt(" #n ")" ::: "memory")
; #define PG8_WAIT_L(n) asm volatile("s_waitcnt lgkmcnt(" #n ")" ::: "memory")
; #define PG8_BAR __builtin_amdgcn_s_barrier()
; #define PG8_SCHED __builtin_amdgcn_sched_barrier(0)
; template <class Epi, class Sched, bool ALIGN_EPI = false, bool SP2 = false>
; __device__ __forceinline__ void gemm_phase(PG8_LAS unsigned char* lds, const Gemm g, const Sched& S, const Epi& E, const int tid) {
;     ...
;             PG8_LDB(B0, 0, 0); PG8_LDB(B1, 0, 1); PG8_SCHED; PG8_LDA(At, 0, 0); PG8_STAGE(PG8_SA(1, 1), a1 + hstep, voffA);
;             PG8_WAIT_V(8); PG8_WAIT_L(0); PG8_BAR; PG8_MMA(0, 0, At, B0); PG8_MMA(0, 1, At, B1); PG8_BAR; PG8_SCHED;
;             PG8_LDA(At, 0, 1); PG8_STAGE(PG8_SB(0, 0), b2, voffB); PG8_STAGE(PG8_SB(0, 1), b2 + hstep, voffB); PG8_STAGE(PG8_SA(0, 0), a2, voffA);
.LBB0_791:
	s_add_u32 s22, s18, 0xfff80080
	s_addc_u32 s23, s19, -1
	s_add_i32 s54, 0, 0x10000
	s_cmp_eq_u32 s53, 28
	s_cselect_b32 s27, s13, s23
	s_cselect_b32 s26, s49, s22
	v_add_u32_e32 v145, s54, v142
	s_cselect_b32 s23, s11, s52
	s_cselect_b32 s22, s50, s51
	s_add_i32 s56, 0, 0x14000
	ds_read_b128 v[146:149], v145
	ds_read_b128 v[150:153], v145 offset:1024
	ds_read_b128 v[154:157], v145 offset:2048
	ds_read_b128 v[158:161], v145 offset:3072
	v_add_u32_e32 v145, s56, v142
	ds_read_b128 v[162:165], v145
	ds_read_b128 v[166:169], v145 offset:1024
	ds_read_b128 v[170:173], v145 offset:2048
	ds_read_b128 v[174:177], v145 offset:3072
	v_lshl_add_u64 v[196:197], s[18:19], 0, v[138:139]
	s_add_i32 m0, s35, 0xc000
	ds_read_b128 v[178:181], v144
	ds_read_b128 v[182:185], v144 offset:1024
	ds_read_b128 v[186:189], v144 offset:2048
	ds_read_b128 v[190:193], v144 offset:3072
	ds_read_b128 v[210:213], v144 offset:4096
	ds_read_b128 v[214:217], v144 offset:5120
	ds_read_b128 v[218:221], v144 offset:6144
	ds_read_b128 v[234:237], v144 offset:7168
	global_load_lds_dwordx4 v[196:197], off
	v_lshl_add_u64 v[196:197], s[18:19], 0, v[140:141]
	s_add_i32 m0, s35, 0xe000
	s_nop 0
	global_load_lds_dwordx4 v[196:197], off
	s_waitcnt vmcnt(8)
	s_waitcnt lgkmcnt(0)
	s_barrier
	s_setprio 1
	s_waitcnt lgkmcnt(0)
	v_mfma_f32_16x16x32_bf16 v[126:129], v[146:149], v[178:181], v[126:129]
	v_mfma_f32_16x16x32_bf16 v[122:125], v[154:157], v[178:181], v[122:125]
	v_mfma_f32_16x16x32_bf16 v[118:121], v[146:149], v[186:189], v[118:121]
	v_mfma_f32_16x16x32_bf16 v[114:117], v[154:157], v[186:189], v[114:117]
	v_mfma_f32_16x16x32_bf16 v[102:105], v[146:149], v[210:213], v[102:105]
	v_mfma_f32_16x16x32_bf16 v[98:101], v[154:157], v[210:213], v[98:101]
	v_mfma_f32_16x16x32_bf16 v[86:89], v[146:149], v[218:221], v[86:89]
	v_mfma_f32_16x16x32_bf16 v[82:85], v[154:157], v[218:221], v[82:85]
	v_mfma_f32_16x16x32_bf16 v[126:129], v[150:153], v[182:185], v[126:129]
	v_mfma_f32_16x16x32_bf16 v[122:125], v[158:161], v[182:185], v[122:125]
	v_mfma_f32_16x16x32_bf16 v[118:121], v[150:153], v[190:193], v[118:121]
	v_mfma_f32_16x16x32_bf16 v[114:117], v[158:161], v[190:193], v[114:117]
	v_mfma_f32_16x16x32_bf16 v[102:105], v[150:153], v[214:217], v[102:105]
	v_mfma_f32_16x16x32_bf16 v[98:101], v[158:161], v[214:217], v[98:101]
	v_mfma_f32_16x16x32_bf16 v[86:89], v[150:153], v[234:237], v[86:89]
	v_mfma_f32_16x16x32_bf16 v[82:85], v[158:161], v[234:237], v[82:85]
	v_mfma_f32_16x16x32_bf16 v[110:113], v[162:165], v[178:181], v[110:113]
	v_mfma_f32_16x16x32_bf16 v[106:109], v[170:173], v[178:181], v[106:109]
	v_mfma_f32_16x16x32_bf16 v[94:97], v[162:165], v[186:189], v[94:97]
	v_mfma_f32_16x16x32_bf16 v[90:93], v[170:173], v[186:189], v[90:93]
	v_mfma_f32_16x16x32_bf16 v[76:79], v[162:165], v[210:213], v[76:79]
	v_mfma_f32_16x16x32_bf16 v[72:75], v[170:173], v[210:213], v[72:75]
	v_mfma_f32_16x16x32_bf16 v[68:71], v[162:165], v[218:221], v[68:71]
	v_mfma_f32_16x16x32_bf16 v[64:67], v[170:173], v[218:221], v[64:67]
	v_mfma_f32_16x16x32_bf16 v[110:113], v[166:169], v[182:185], v[110:113]
	v_mfma_f32_16x16x32_bf16 v[106:109], v[174:177], v[182:185], v[106:109]
	v_mfma_f32_16x16x32_bf16 v[94:97], v[166:169], v[190:193], v[94:97]
	v_mfma_f32_16x16x32_bf16 v[90:93], v[174:177], v[190:193], v[90:93]
	v_mfma_f32_16x16x32_bf16 v[76:79], v[166:169], v[214:217], v[76:79]
	v_mfma_f32_16x16x32_bf16 v[72:75], v[174:177], v[214:217], v[72:75]
	v_mfma_f32_16x16x32_bf16 v[68:71], v[166:169], v[234:237], v[68:71]
	v_mfma_f32_16x16x32_bf16 v[64:67], v[174:177], v[234:237], v[64:67]
	s_setprio 0
	s_barrier
	s_add_i32 s54, s54, s34
	v_lshl_add_u64 v[196:197], s[22:23], 0, v[134:135]
	s_mov_b32 m0, s54
	ds_read_b128 v[178:181], v144 offset:16384
	ds_read_b128 v[182:185], v144 offset:17408
	ds_read_b128 v[186:189], v144 offset:18432
	ds_read_b128 v[190:193], v144 offset:19456
	ds_read_b128 v[210:213], v144 offset:20480
	ds_read_b128 v[214:217], v144 offset:21504
	ds_read_b128 v[218:221], v144 offset:22528
	ds_read_b128 v[234:237], v144 offset:23552
	global_load_lds_dwordx4 v[196:197], off
	s_add_i32 m0, s54, 0x2000
	s_add_u32 s54, s22, 0x80000
	v_lshl_add_u64 v[198:199], s[22:23], 0, v[130:131]
	s_addc_u32 s55, s23, 0
	s_add_i32 s56, s56, s34
	global_load_lds_dwordx4 v[198:199], off
	v_lshl_add_u64 v[206:207], s[54:55], 0, v[134:135]
	s_mov_b32 m0, s56
	v_lshl_add_u64 v[238:239], s[26:27], 0, v[132:133]
	global_load_lds_dwordx4 v[206:207], off
	v_lshl_add_u64 v[206:207], s[54:55], 0, v[130:131]
	s_add_i32 m0, s56, 0x2000
	s_nop 0
	global_load_lds_dwordx4 v[206:207], off
	v_lshl_add_u64 v[206:207], s[26:27], 0, v[136:137]
	s_mov_b32 m0, s35
	s_nop 0
	global_load_lds_dwordx4 v[206:207], off
	s_mov_b32 m0, s36
	s_nop 0
	global_load_lds_dwordx4 v[238:239], off
	s_waitcnt vmcnt(8)
	s_waitcnt lgkmcnt(0)
	s_barrier
; #define PG8_STAGE(bufoff, gbase, voff) do { _Pragma("unroll") for (int _i = 0; _i < 2; ++_i) \
;         __builtin_amdgcn_global_load_lds((const unsigned*)((const char*)(gbase) + (voff)[_i]), (PG8_LAS unsigned*)(lds + (bufoff) + ldsw + _i * 8192), 16, 0, 0); } while (0)
; #define PG8_LDA(dst, b, h) do { _Pragma("unroll") for (int m = 0; m < 4; ++m) _Pragma("unroll") for (int k = 0; k < 2; ++k) dst[m][k] = *(const PG8_LAS bf16x8*)(lds + PG8_SA(b, h) + aoff + m * 2048 + k * 1024); } while (0)
; #define PG8_LDB(dst, b, h) do { _Pragma("unroll") for (int n = 0; n < 2; ++n) _Pragma("unroll") for (int k = 0; k < 2; ++k) dst[n][k] = *(const PG8_LAS bf16x8*)(lds + PG8_SB(b, h) + boff + n * 2048 + k * 1024); } while (0)
; #define PG8_MMA(ai, bj, At, Bt) do { __builtin_amdgcn_s_setprio(1); _Pragma("unroll") for (int m = 0; m < 4; ++m) _Pragma("unroll") for (int n = 0; n < 2; ++n) _Pragma("unroll") for (int k = 0; k < 2; ++k) \
;         acc[ai][bj][m][n] = __builtin_amdgcn_mfma_f32_16x16x32_bf16(Bt[n][k], At[m][k], acc[ai][bj][m][n], 0, 0, 0); __builtin_amdgcn_s_setprio(0); } while (0)
; #define PG8_WAIT_V(n) asm volatile("s_waitcnt vmcnt(" #n ")" ::: "memory")
; #define PG8_WAIT_L(n) asm volatile("s_waitcnt lgkmcnt(" #n ")" ::: "memory")
; #define PG8_BAR __builtin_amdgcn_s_barrier()
; #define PG8_SCHED __builtin_amdgcn_sched_barrier(0)
; template <class Epi, class Sched, bool ALIGN_EPI = false, bool SP2 = false>
; __device__ __forceinline__ void gemm_phase(PG8_LAS unsigned char* lds, const Gemm g, const Sched& S, const Epi& E, const int tid) {
;     ...
;             PG8_WAIT_V(8); PG8_WAIT_L(0); PG8_BAR; PG8_MMA(1, 0, At, B0); PG8_MMA(1, 1, At, B1); PG8_BAR; PG8_SCHED;
;             PG8_LDB(B0, 1, 0); PG8_LDB(B1, 1, 1); PG8_SCHED; PG8_LDA(At, 1, 0); PG8_STAGE(PG8_SA(0, 1), a2 + hstep, voffA);
;             PG8_WAIT_V(8); PG8_WAIT_L(0); PG8_BAR; PG8_MMA(0, 0, At, B0); PG8_MMA(0, 1, At, B1); PG8_BAR; PG8_SCHED;
	s_setprio 1
	s_waitcnt lgkmcnt(0)
	v_mfma_f32_16x16x32_bf16 v[60:63], v[146:149], v[178:181], v[60:63]
	v_mfma_f32_16x16x32_bf16 v[56:59], v[154:157], v[178:181], v[56:59]
	v_mfma_f32_16x16x32_bf16 v[52:55], v[146:149], v[186:189], v[52:55]
	v_mfma_f32_16x16x32_bf16 v[48:51], v[154:157], v[186:189], v[48:51]
	v_mfma_f32_16x16x32_bf16 v[36:39], v[146:149], v[210:213], v[36:39]
	v_mfma_f32_16x16x32_bf16 v[32:35], v[154:157], v[210:213], v[32:35]
	v_mfma_f32_16x16x32_bf16 v[20:23], v[146:149], v[218:221], v[20:23]
	v_mfma_f32_16x16x32_bf16 v[16:19], v[154:157], v[218:221], v[16:19]
	v_mfma_f32_16x16x32_bf16 v[60:63], v[150:153], v[182:185], v[60:63]
	v_mfma_f32_16x16x32_bf16 v[56:59], v[158:161], v[182:185], v[56:59]
	v_mfma_f32_16x16x32_bf16 v[52:55], v[150:153], v[190:193], v[52:55]
	v_mfma_f32_16x16x32_bf16 v[48:51], v[158:161], v[190:193], v[48:51]
	v_mfma_f32_16x16x32_bf16 v[36:39], v[150:153], v[214:217], v[36:39]
	v_mfma_f32_16x16x32_bf16 v[32:35], v[158:161], v[214:217], v[32:35]
	v_mfma_f32_16x16x32_bf16 v[20:23], v[150:153], v[234:237], v[20:23]
	v_mfma_f32_16x16x32_bf16 v[16:19], v[158:161], v[234:237], v[16:19]
	v_mfma_f32_16x16x32_bf16 v[44:47], v[162:165], v[178:181], v[44:47]
	v_mfma_f32_16x16x32_bf16 v[40:43], v[170:173], v[178:181], v[40:43]
	v_mfma_f32_16x16x32_bf16 v[28:31], v[162:165], v[186:189], v[28:31]
	v_mfma_f32_16x16x32_bf16 v[24:27], v[170:173], v[186:189], v[24:27]
	v_mfma_f32_16x16x32_bf16 v[12:15], v[162:165], v[210:213], v[12:15]
	v_mfma_f32_16x16x32_bf16 v[8:11], v[170:173], v[210:213], v[8:11]
	v_mfma_f32_16x16x32_bf16 v[4:7], v[162:165], v[218:221], v[4:7]
	v_mfma_f32_16x16x32_bf16 v[0:3], v[170:173], v[218:221], v[0:3]
	v_mfma_f32_16x16x32_bf16 v[44:47], v[166:169], v[182:185], v[44:47]
	v_mfma_f32_16x16x32_bf16 v[40:43], v[174:177], v[182:185], v[40:43]
	v_mfma_f32_16x16x32_bf16 v[28:31], v[166:169], v[190:193], v[28:31]
	v_mfma_f32_16x16x32_bf16 v[24:27], v[174:177], v[190:193], v[24:27]
	v_mfma_f32_16x16x32_bf16 v[12:15], v[166:169], v[214:217], v[12:15]
	v_mfma_f32_16x16x32_bf16 v[8:11], v[174:177], v[214:217], v[8:11]
	v_mfma_f32_16x16x32_bf16 v[4:7], v[166:169], v[234:237], v[4:7]
	v_mfma_f32_16x16x32_bf16 v[0:3], v[174:177], v[234:237], v[0:3]
	s_setprio 0
	s_barrier
	s_add_i32 s54, 0, 0x18000
	v_add_u32_e32 v145, s54, v142
	s_add_i32 s55, 0, 0x1c000
	ds_read_b128 v[146:149], v145
	ds_read_b128 v[150:153], v145 offset:1024
	ds_read_b128 v[154:157], v145 offset:2048
	ds_read_b128 v[158:161], v145 offset:3072
	v_add_u32_e32 v145, s55, v142
	ds_read_b128 v[162:165], v145
	ds_read_b128 v[166:169], v145 offset:1024
	ds_read_b128 v[170:173], v145 offset:2048
	ds_read_b128 v[174:177], v145 offset:3072
	s_add_u32 s26, s26, 0x80000
	s_addc_u32 s27, s27, 0
	s_mov_b32 m0, s42
	v_lshl_add_u64 v[240:241], s[26:27], 0, v[136:137]
	ds_read_b128 v[178:181], v144 offset:32768
	ds_read_b128 v[182:185], v144 offset:33792
	ds_read_b128 v[186:189], v144 offset:34816
	ds_read_b128 v[190:193], v144 offset:35840
	ds_read_b128 v[210:213], v144 offset:36864
	ds_read_b128 v[214:217], v144 offset:37888
	ds_read_b128 v[218:221], v144 offset:38912
	ds_read_b128 v[234:237], v144 offset:39936
	global_load_lds_dwordx4 v[240:241], off
	v_lshl_add_u64 v[240:241], s[26:27], 0, v[132:133]
	s_mov_b32 m0, s43
	s_nop 0
	global_load_lds_dwordx4 v[240:241], off
	s_waitcnt vmcnt(8)
	s_waitcnt lgkmcnt(0)
	s_barrier
	s_setprio 1
	s_waitcnt lgkmcnt(0)
	v_mfma_f32_16x16x32_bf16 v[126:129], v[146:149], v[178:181], v[126:129]
	v_mfma_f32_16x16x32_bf16 v[122:125], v[154:157], v[178:181], v[122:125]
	v_mfma_f32_16x16x32_bf16 v[118:121], v[146:149], v[186:189], v[118:121]
	v_mfma_f32_16x16x32_bf16 v[114:117], v[154:157], v[186:189], v[114:117]
	v_mfma_f32_16x16x32_bf16 v[102:105], v[146:149], v[210:213], v[102:105]
	v_mfma_f32_16x16x32_bf16 v[98:101], v[154:157], v[210:213], v[98:101]
	v_mfma_f32_16x16x32_bf16 v[86:89], v[146:149], v[218:221], v[86:89]
	v_mfma_f32_16x16x32_bf16 v[82:85], v[154:157], v[218:221], v[82:85]
	v_mfma_f32_16x16x32_bf16 v[126:129], v[150:153], v[182:185], v[126:129]
	v_mfma_f32_16x16x32_bf16 v[122:125], v[158:161], v[182:185], v[122:125]
	v_mfma_f32_16x16x32_bf16 v[118:121], v[150:153], v[190:193], v[118:121]
	v_mfma_f32_16x16x32_bf16 v[114:117], v[158:161], v[190:193], v[114:117]
	v_mfma_f32_16x16x32_bf16 v[102:105], v[150:153], v[214:217], v[102:105]
	v_mfma_f32_16x16x32_bf16 v[98:101], v[158:161], v[214:217], v[98:101]
	v_mfma_f32_16x16x32_bf16 v[86:89], v[150:153], v[234:237], v[86:89]
	v_mfma_f32_16x16x32_bf16 v[82:85], v[158:161], v[234:237], v[82:85]
	v_mfma_f32_16x16x32_bf16 v[110:113], v[162:165], v[178:181], v[110:113]
	v_mfma_f32_16x16x32_bf16 v[106:109], v[170:173], v[178:181], v[106:109]
	v_mfma_f32_16x16x32_bf16 v[94:97], v[162:165], v[186:189], v[94:97]
	v_mfma_f32_16x16x32_bf16 v[90:93], v[170:173], v[186:189], v[90:93]
	v_mfma_f32_16x16x32_bf16 v[76:79], v[162:165], v[210:213], v[76:79]
	v_mfma_f32_16x16x32_bf16 v[72:75], v[170:173], v[210:213], v[72:75]
	v_mfma_f32_16x16x32_bf16 v[68:71], v[162:165], v[218:221], v[68:71]
	v_mfma_f32_16x16x32_bf16 v[64:67], v[170:173], v[218:221], v[64:67]
	v_mfma_f32_16x16x32_bf16 v[110:113], v[166:169], v[182:185], v[110:113]
	v_mfma_f32_16x16x32_bf16 v[106:109], v[174:177], v[182:185], v[106:109]
	v_mfma_f32_16x16x32_bf16 v[94:97], v[166:169], v[190:193], v[94:97]
	v_mfma_f32_16x16x32_bf16 v[90:93], v[174:177], v[190:193], v[90:93]
	v_mfma_f32_16x16x32_bf16 v[76:79], v[166:169], v[214:217], v[76:79]
	v_mfma_f32_16x16x32_bf16 v[72:75], v[174:177], v[214:217], v[72:75]
	v_mfma_f32_16x16x32_bf16 v[68:71], v[166:169], v[234:237], v[68:71]
	v_mfma_f32_16x16x32_bf16 v[64:67], v[174:177], v[234:237], v[64:67]
	s_setprio 0
	s_barrier
; #define PG8_STAGE(bufoff, gbase, voff) do { _Pragma("unroll") for (int _i = 0; _i < 2; ++_i) \
;         __builtin_amdgcn_global_load_lds((const unsigned*)((const char*)(gbase) + (voff)[_i]), (PG8_LAS unsigned*)(lds + (bufoff) + ldsw + _i * 8192), 16, 0, 0); } while (0)
; #define PG8_LDA(dst, b, h) do { _Pragma("unroll") for (int m = 0; m < 4; ++m) _Pragma("unroll") for (int k = 0; k < 2; ++k) dst[m][k] = *(const PG8_LAS bf16x8*)(lds + PG8_SA(b, h) + aoff + m * 2048 + k * 1024); } while (0)
; #define PG8_MMA(ai, bj, At, Bt) do { __builtin_amdgcn_s_setprio(1); _Pragma("unroll") for (int m = 0; m < 4; ++m) _Pragma("unroll") for (int n = 0; n < 2; ++n) _Pragma("unroll") for (int k = 0; k < 2; ++k) \
;         acc[ai][bj][m][n] = __builtin_amdgcn_mfma_f32_16x16x32_bf16(Bt[n][k], At[m][k], acc[ai][bj][m][n], 0, 0, 0); __builtin_amdgcn_s_setprio(0); } while (0)
; #define PG8_WAIT_V(n) asm volatile("s_waitcnt vmcnt(" #n ")" ::: "memory")
; #define PG8_WAIT_L(n) asm volatile("s_waitcnt lgkmcnt(" #n ")" ::: "memory")
; #define PG8_BAR __builtin_amdgcn_s_barrier()
; #define PG8_SCHED __builtin_amdgcn_sched_barrier(0)
; template <class Epi, class Sched, bool ALIGN_EPI = false, bool SP2 = false>
; __device__ __forceinline__ void gemm_phase(PG8_LAS unsigned char* lds, const Gemm g, const Sched& S, const Epi& E, const int tid) {
;     ...
;             PG8_LDA(At, 1, 1); PG8_STAGE(PG8_SB(1, 0), b3, voffB); PG8_STAGE(PG8_SB(1, 1), b3 + hstep, voffB); PG8_STAGE(PG8_SA(1, 0), a3, voffA);
;             PG8_WAIT_V(8); PG8_WAIT_L(0); PG8_BAR; PG8_MMA(1, 0, At, B0); PG8_MMA(1, 1, At, B1); PG8_BAR; PG8_SCHED;
;     ...
;         if constexpr (ALIGN_EPI) { if (wr == 0) PG8_BAR; }
	s_add_i32 s26, s54, s34
	v_lshl_add_u64 v[196:197], v[196:197], 0, s[20:21]
	s_mov_b32 m0, s26
	ds_read_b128 v[178:181], v144 offset:49152
	ds_read_b128 v[182:185], v144 offset:50176
	ds_read_b128 v[186:189], v144 offset:51200
	ds_read_b128 v[190:193], v144 offset:52224
	ds_read_b128 v[210:213], v144 offset:53248
	ds_read_b128 v[214:217], v144 offset:54272
	ds_read_b128 v[218:221], v144 offset:55296
	ds_read_b128 v[234:237], v144 offset:56320
	global_load_lds_dwordx4 v[196:197], off
	s_add_i32 m0, s26, 0x2000
	s_add_u32 s22, s22, 0x80080
	v_lshl_add_u64 v[196:197], v[198:199], 0, s[20:21]
	s_addc_u32 s23, s23, 0
	s_add_i32 s26, s55, s34
	global_load_lds_dwordx4 v[196:197], off
	v_lshl_add_u64 v[196:197], s[22:23], 0, v[134:135]
	s_mov_b32 m0, s26
	s_nop 0
	global_load_lds_dwordx4 v[196:197], off
	v_lshl_add_u64 v[196:197], s[22:23], 0, v[130:131]
	s_add_i32 m0, s26, 0x2000
	s_nop 0
	global_load_lds_dwordx4 v[196:197], off
	v_lshl_add_u64 v[196:197], v[206:207], 0, s[20:21]
	s_mov_b32 m0, s44
	s_nop 0
	global_load_lds_dwordx4 v[196:197], off
	v_lshl_add_u64 v[196:197], v[238:239], 0, s[20:21]
	s_mov_b32 m0, s45
	s_nop 0
	global_load_lds_dwordx4 v[196:197], off
	s_waitcnt vmcnt(8)
	s_waitcnt lgkmcnt(0)
	s_barrier
	s_setprio 1
	s_waitcnt lgkmcnt(0)
	v_mfma_f32_16x16x32_bf16 v[60:63], v[146:149], v[178:181], v[60:63]
	v_mfma_f32_16x16x32_bf16 v[56:59], v[154:157], v[178:181], v[56:59]
	v_mfma_f32_16x16x32_bf16 v[52:55], v[146:149], v[186:189], v[52:55]
	v_mfma_f32_16x16x32_bf16 v[48:51], v[154:157], v[186:189], v[48:51]
	v_mfma_f32_16x16x32_bf16 v[36:39], v[146:149], v[210:213], v[36:39]
	v_mfma_f32_16x16x32_bf16 v[32:35], v[154:157], v[210:213], v[32:35]
	v_mfma_f32_16x16x32_bf16 v[20:23], v[146:149], v[218:221], v[20:23]
	v_mfma_f32_16x16x32_bf16 v[16:19], v[154:157], v[218:221], v[16:19]
	v_mfma_f32_16x16x32_bf16 v[60:63], v[150:153], v[182:185], v[60:63]
	v_mfma_f32_16x16x32_bf16 v[56:59], v[158:161], v[182:185], v[56:59]
	v_mfma_f32_16x16x32_bf16 v[52:55], v[150:153], v[190:193], v[52:55]
	v_mfma_f32_16x16x32_bf16 v[48:51], v[158:161], v[190:193], v[48:51]
	v_mfma_f32_16x16x32_bf16 v[36:39], v[150:153], v[214:217], v[36:39]
	v_mfma_f32_16x16x32_bf16 v[32:35], v[158:161], v[214:217], v[32:35]
	v_mfma_f32_16x16x32_bf16 v[20:23], v[150:153], v[234:237], v[20:23]
	v_mfma_f32_16x16x32_bf16 v[16:19], v[158:161], v[234:237], v[16:19]
	v_mfma_f32_16x16x32_bf16 v[44:47], v[162:165], v[178:181], v[44:47]
	v_mfma_f32_16x16x32_bf16 v[40:43], v[170:173], v[178:181], v[40:43]
	v_mfma_f32_16x16x32_bf16 v[28:31], v[162:165], v[186:189], v[28:31]
	v_mfma_f32_16x16x32_bf16 v[24:27], v[170:173], v[186:189], v[24:27]
	v_mfma_f32_16x16x32_bf16 v[12:15], v[162:165], v[210:213], v[12:15]
	v_mfma_f32_16x16x32_bf16 v[8:11], v[170:173], v[210:213], v[8:11]
	v_mfma_f32_16x16x32_bf16 v[4:7], v[162:165], v[218:221], v[4:7]
	v_mfma_f32_16x16x32_bf16 v[0:3], v[170:173], v[218:221], v[0:3]
	v_mfma_f32_16x16x32_bf16 v[44:47], v[166:169], v[182:185], v[44:47]
	v_mfma_f32_16x16x32_bf16 v[40:43], v[174:177], v[182:185], v[40:43]
	v_mfma_f32_16x16x32_bf16 v[28:31], v[166:169], v[190:193], v[28:31]
	v_mfma_f32_16x16x32_bf16 v[24:27], v[174:177], v[190:193], v[24:27]
	v_mfma_f32_16x16x32_bf16 v[12:15], v[166:169], v[214:217], v[12:15]
	v_mfma_f32_16x16x32_bf16 v[8:11], v[174:177], v[214:217], v[8:11]
	v_mfma_f32_16x16x32_bf16 v[4:7], v[166:169], v[234:237], v[4:7]
	v_mfma_f32_16x16x32_bf16 v[0:3], v[174:177], v[234:237], v[0:3]
	s_setprio 0
	s_barrier
	s_add_i32 s53, s53, 2
	s_add_u32 s18, s18, 0x100
	s_addc_u32 s19, s19, 0
	s_add_u32 s51, s51, 0x100
	s_addc_u32 s52, s52, 0
	s_cmp_gt_u32 s53, 29
	s_cbranch_scc0 .LBB0_791
	s_and_b64 vcc, exec, s[8:9]
	s_cbranch_vccz .LBB0_794
	s_barrier
